# static mapping like baseline, ring 16 with 8KiB bursts (no dynamic queue)
# baseline (speedup 1.0000x reference)
.Lk1_scan:
	s_load_dwordx2 s[4:5], s[0:1], 0x0
	s_load_dwordx4 s[8:11], s[0:1], 0x20
	s_load_dwordx2 s[12:13], s[0:1], 0x30
	v_and_b32_e32 v6, 63, v0
	v_readfirstlane_b32 s3, v0
	v_lshlrev_b32_e32 v1, 4, v6
	v_lshlrev_b32_e32 v2, 2, v6
	v_or_b32_e32 v3, 1, v2
	v_or_b32_e32 v4, 2, v2
	v_or_b32_e32 v5, 3, v2
	s_lshr_b32 s3, s3, 6
	s_sub_u32 s16, s2, 0x60
	s_lshl_b32 s16, s16, 2
	s_add_u32 s16, s16, s3
	s_mul_i32 s17, s16, 0x48000
	s_lshr_b32 s18, s17, 2
	s_lshl_b32 s24, s3, 13
	s_mov_b32 s25, s24
	s_mov_b32 s28, s24
	s_mov_b32 s36, 0
	v_mov_b32_e32 v21, 1
	s_mov_b32 s27, 0
	s_mov_b32 s29, 0x55555556
	s_mov_b32 s31, 0xc0000
	s_waitcnt lgkmcnt(0)
	s_add_u32 s6, s4, s17
	s_addc_u32 s7, s5, 0
	global_load_dwordx4 v[28:31], v1, s[6:7] nt
	s_add_u32 s6, s6, 0x400
	s_addc_u32 s7, s7, 0
	global_load_dwordx4 v[32:35], v1, s[6:7] nt
	s_add_u32 s6, s6, 0x400
	s_addc_u32 s7, s7, 0
	global_load_dwordx4 v[36:39], v1, s[6:7] nt
	s_add_u32 s6, s6, 0x400
	s_addc_u32 s7, s7, 0
	global_load_dwordx4 v[40:43], v1, s[6:7] nt
	s_add_u32 s6, s6, 0x400
	s_addc_u32 s7, s7, 0
	global_load_dwordx4 v[44:47], v1, s[6:7] nt
	s_add_u32 s6, s6, 0x400
	s_addc_u32 s7, s7, 0
	global_load_dwordx4 v[48:51], v1, s[6:7] nt
	s_add_u32 s6, s6, 0x400
	s_addc_u32 s7, s7, 0
	global_load_dwordx4 v[52:55], v1, s[6:7] nt
	s_add_u32 s6, s6, 0x400
	s_addc_u32 s7, s7, 0
	global_load_dwordx4 v[56:59], v1, s[6:7] nt
	s_add_u32 s6, s6, 0x400
	s_addc_u32 s7, s7, 0
	global_load_dwordx4 v[60:63], v1, s[6:7] nt
	s_add_u32 s6, s6, 0x400
	s_addc_u32 s7, s7, 0
	global_load_dwordx4 v[64:67], v1, s[6:7] nt
	s_add_u32 s6, s6, 0x400
	s_addc_u32 s7, s7, 0
	global_load_dwordx4 v[68:71], v1, s[6:7] nt
	s_add_u32 s6, s6, 0x400
	s_addc_u32 s7, s7, 0
	global_load_dwordx4 v[72:75], v1, s[6:7] nt
	s_add_u32 s6, s6, 0x400
	s_addc_u32 s7, s7, 0
	global_load_dwordx4 v[76:79], v1, s[6:7] nt
	s_add_u32 s6, s6, 0x400
	s_addc_u32 s7, s7, 0
	global_load_dwordx4 v[80:83], v1, s[6:7] nt
	s_add_u32 s6, s6, 0x400
	s_addc_u32 s7, s7, 0
	global_load_dwordx4 v[84:87], v1, s[6:7] nt
	s_add_u32 s6, s6, 0x400
	s_addc_u32 s7, s7, 0
	global_load_dwordx4 v[88:91], v1, s[6:7] nt
	s_add_u32 s6, s6, 0x400
	s_addc_u32 s7, s7, 0
	s_mov_b32 s26, 18

.Lk1_contm_15:
	global_load_dwordx4 v[60:63], v1, s[6:7] nt
	s_add_u32 s6, s6, 0x400
	s_addc_u32 s7, s7, 0
	global_load_dwordx4 v[64:67], v1, s[6:7] nt
	s_add_u32 s6, s6, 0x400
	s_addc_u32 s7, s7, 0
	global_load_dwordx4 v[68:71], v1, s[6:7] nt
	s_add_u32 s6, s6, 0x400
	s_addc_u32 s7, s7, 0
	global_load_dwordx4 v[72:75], v1, s[6:7] nt
	s_add_u32 s6, s6, 0x400
	s_addc_u32 s7, s7, 0
	global_load_dwordx4 v[76:79], v1, s[6:7] nt
	s_add_u32 s6, s6, 0x400
	s_addc_u32 s7, s7, 0
	global_load_dwordx4 v[80:83], v1, s[6:7] nt
	s_add_u32 s6, s6, 0x400
	s_addc_u32 s7, s7, 0
	global_load_dwordx4 v[84:87], v1, s[6:7] nt
	s_add_u32 s6, s6, 0x400
	s_addc_u32 s7, s7, 0
	global_load_dwordx4 v[88:91], v1, s[6:7] nt
	s_add_u32 s6, s6, 0x400
	s_addc_u32 s7, s7, 0
	s_add_u32 s18, s18, 0x1000
	s_sub_u32 s26, s26, 1
	s_cmp_lg_u32 s26, 1
	s_cbranch_scc1 .Lk1_main
	s_waitcnt vmcnt(15)
	v_or3_b32 v12, v28, v29, v30
	v_or_b32_e32 v12, v12, v31
	v_cmp_ne_u32_e32 vcc, 0, v12
	s_cbranch_vccnz .Lk1_hitl_0
